# v32: attention-phase conversion split 60/38/24/24 per workgroup class (was 72/50/12/12)
# baseline (speedup 1.0000x reference)
; #define LAS __attribute__((address_space(3)))
; __global__ void __launch_bounds__(NWAVES * 64, 2) mega_fwd(Args args) {
;     ...
;         if (F.G == 256) { const int pq = blockIdx.x, bg_ = (pq & 7) * 2 + ((pq >> 3) & 1), g_ = bg_ & 3, li = (bg_ >> 2) * 16 + (pq >> 4);
;             if (g_ < 2) { const int cnt = g_ == 0 ? TR_AT0 : TR_AT1, first = g_ == 0 ? li * TR_AT0 : 64 * TR_AT0 + li * TR_AT1;
;                 tr_run<2>(F, first + F.wave, first + cnt, NWAVES, (LAS float*)(F.lds + RING_OFF + F.wave * 16384)); }
.LBB0_1331:
	s_mov_b64 s[86:87], s[18:19]
	v_readlane_b32 s66, v248, 20
	s_cmpk_eq_i32 s89, 0x100
	v_readlane_b32 s92, v248, 14
	s_mov_b64 s[84:85], s[16:17]
	s_mov_b64 s[82:83], s[14:15]
	s_mov_b64 s[80:81], s[12:13]
	s_mov_b64 s[78:79], s[10:11]
	v_readlane_b32 s67, v248, 21
	s_waitcnt lgkmcnt(0)
	s_barrier
	s_cbranch_scc0 .LBB0_1489
	v_readlane_b32 s0, v249, 37
	s_and_b32 s4, s0, 48
	s_ashr_i32 s0, s92, 4
	s_add_i32 s4, s4, s0
	s_bfe_u32 s2, s92, 0x10003
	s_and_b32 s0, s92, 1
	s_lshl_b32 s0, s0, 1
	s_or_b32 s2, s2, s0
	s_mov_b32 s17, 60
	s_mov_b32 s16, 0
	s_cmp_eq_u32 s2, 1
	s_cselect_b32 s17, 38, s17
	s_cselect_b32 s16, 0xf00, s16
	s_cmp_eq_u32 s2, 2
	s_cselect_b32 s17, 24, s17
	s_cselect_b32 s16, 0x1880, s16
	s_cmp_eq_u32 s2, 3
	s_cselect_b32 s17, 24, s17
	s_cselect_b32 s16, 0x1e80, s16
	s_mul_i32 s0, s4, s17
	s_add_i32 s16, s16, s0
	v_readlane_b32 s0, v249, 36
	s_cmp_lt_u32 s0, s17
	s_cselect_b64 s[14:15], -1, 0
	s_and_b64 vcc, exec, s[14:15]
	s_cbranch_vccnz .LBB0_1339
	v_lshrrev_b32_e32 v130, 3, v180
	v_lshlrev_b32_e32 v1, 2, v0
	v_and_b32_e32 v132, 28, v1
	v_mov_b32_e32 v133, 0
	v_or_b32_e32 v134, 64, v130
	s_mov_b64 s[0:1], 0
	s_branch .LBB0_1340
